# serialized load/wait chains removed: LN1 K-split rows, diff epilogue gain loads, diff/swa max-bias loads hoisted; gemm2 epilogue counted vmcnt (no store-ack waits)
# speedup vs baseline: 1.0397x; 1.0181x over previous
;     ...
;     for (int i = tid; i < 4 * 129; i += NTHR) { const int h = i / 129, n = i % 129; btab[h * 132 + n] = p.in[I_RELB][t5_bucket(n) * 8 + 4 + h] * 5.656854249492381f; }
;     if (tid < 4) { float bx = -1e30f; for (int n = 0; n < 32; ++n) bx = fmaxf(bx, p.in[I_RELB][n * 8 + 4 + tid]); btab[tid * 132 + 129] = bx * 5.656854249492381f; }
.LBB0_765:
	s_or_b64 exec, exec, s[0:1]
	v_cmp_gt_i32_e32 vcc, 4, v30
	s_and_saveexec_b64 s[0:1], vcc
	s_cbranch_execz .LBB0_767
	v_readlane_b32 s48, v253, 12
	v_ashrrev_i32_e32 v31, 31, v30
	v_readlane_b32 s60, v253, 24
	v_readlane_b32 s61, v253, 25
	s_mov_b32 s2, 0xf149f2ca
	v_readlane_b32 s49, v253, 13
	v_lshl_add_u64 v[2:3], v[30:31], 2, s[60:61]
	global_load_dword v0, v[2:3], off offset:16
	global_load_dword v4, v[2:3], off offset:48
	global_load_dword v6, v[2:3], off offset:80
	global_load_dword v7, v[2:3], off offset:112
	global_load_dword v8, v[2:3], off offset:144
	global_load_dword v9, v[2:3], off offset:176
	global_load_dword v10, v[2:3], off offset:208
	global_load_dword v11, v[2:3], off offset:240
	global_load_dword v12, v[2:3], off offset:272
	global_load_dword v13, v[2:3], off offset:304
	global_load_dword v14, v[2:3], off offset:336
	global_load_dword v15, v[2:3], off offset:368
	global_load_dword v16, v[2:3], off offset:400
	global_load_dword v17, v[2:3], off offset:432
	global_load_dword v18, v[2:3], off offset:464
	global_load_dword v19, v[2:3], off offset:496
	global_load_dword v20, v[2:3], off offset:528
	global_load_dword v21, v[2:3], off offset:560
	global_load_dword v22, v[2:3], off offset:592
	global_load_dword v23, v[2:3], off offset:624
	global_load_dword v24, v[2:3], off offset:656
	global_load_dword v25, v[2:3], off offset:688
	global_load_dword v26, v[2:3], off offset:720
	global_load_dword v27, v[2:3], off offset:752
	global_load_dword v28, v[2:3], off offset:784
	global_load_dword v29, v[2:3], off offset:816
	global_load_dword v33, v[2:3], off offset:848
	global_load_dword v34, v[2:3], off offset:880
	global_load_dword v35, v[2:3], off offset:912
	global_load_dword v36, v[2:3], off offset:944
	global_load_dword v37, v[2:3], off offset:976
	global_load_dword v38, v[2:3], off offset:1008
	v_readlane_b32 s50, v253, 14
	v_readlane_b32 s51, v253, 15
	v_readlane_b32 s52, v253, 16
	v_readlane_b32 s53, v253, 17
	v_readlane_b32 s54, v253, 18
	v_readlane_b32 s55, v253, 19
	v_readlane_b32 s56, v253, 20
	v_readlane_b32 s57, v253, 21
	v_readlane_b32 s58, v253, 22
	v_readlane_b32 s59, v253, 23
	v_readlane_b32 s62, v253, 26
	v_readlane_b32 s63, v253, 27
	s_waitcnt vmcnt(0)
	v_max3_f32 v0, v0, s2, v4
	v_mov_b32_e32 v4, v6
	v_mov_b32_e32 v5, v7
	s_movk_i32 s2, 0x210
	s_waitcnt vmcnt(0)
	v_max3_f32 v0, v0, v4, v5
	v_mov_b32_e32 v4, v8
	v_mov_b32_e32 v5, v9
	s_waitcnt vmcnt(0)
	v_max3_f32 v0, v0, v4, v5
	v_mov_b32_e32 v4, v10
	v_mov_b32_e32 v5, v11
	s_waitcnt vmcnt(0)
	v_max3_f32 v0, v0, v4, v5
	v_mov_b32_e32 v4, v12
	v_mov_b32_e32 v5, v13
	s_waitcnt vmcnt(0)
	v_max3_f32 v0, v0, v4, v5
	v_mov_b32_e32 v4, v14
	v_mov_b32_e32 v5, v15
	s_waitcnt vmcnt(0)
	v_max3_f32 v0, v0, v4, v5
	v_mov_b32_e32 v4, v16
	v_mov_b32_e32 v5, v17
	s_waitcnt vmcnt(0)
	v_max3_f32 v0, v0, v4, v5
	v_mov_b32_e32 v4, v18
	v_mov_b32_e32 v5, v19
	s_waitcnt vmcnt(0)
	v_max3_f32 v0, v0, v4, v5
	v_mov_b32_e32 v4, v20
	v_mov_b32_e32 v5, v21
	s_waitcnt vmcnt(0)
	v_max3_f32 v0, v0, v4, v5
	v_mov_b32_e32 v4, v22
	v_mov_b32_e32 v5, v23
	s_waitcnt vmcnt(0)
	v_max3_f32 v0, v0, v4, v5
	v_mov_b32_e32 v4, v24
	v_mov_b32_e32 v5, v25
	s_waitcnt vmcnt(0)
	v_max3_f32 v0, v0, v4, v5
	v_mov_b32_e32 v4, v26
	v_mov_b32_e32 v5, v27
	s_waitcnt vmcnt(0)
	v_max3_f32 v0, v0, v4, v5
	v_mov_b32_e32 v4, v28
	v_mov_b32_e32 v5, v29
	s_waitcnt vmcnt(0)
	v_max3_f32 v0, v0, v4, v5
	v_mov_b32_e32 v4, v33
	v_mov_b32_e32 v5, v34
	s_waitcnt vmcnt(0)
	v_max3_f32 v0, v0, v4, v5
	v_mov_b32_e32 v4, v35
	v_mov_b32_e32 v5, v36
	s_waitcnt vmcnt(0)
	v_max3_f32 v0, v0, v4, v5
	v_mov_b32_e32 v4, v37
	s_nop 0
	v_mov_b32_e32 v2, v38
	s_waitcnt vmcnt(0)
	v_max3_f32 v0, v0, v4, v2
	v_mul_lo_u32 v2, v30, s2
	v_mul_f32_e32 v0, 0x40b504f3, v0
	v_add_u32_e32 v2, 0, v2
	ds_write_b32 v2, v0 offset:516

; __device__ __forceinline__ float frsq(float x) { return __builtin_amdgcn_rsqf(x); }
; __device__ __forceinline__ int lt_tid(int wv) { int ln; asm volatile("v_mbcnt_lo_u32_b32 %0, -1, 0\n\tv_mbcnt_hi_u32_b32 %0, -1, %0" : "=v"(ln)); return (wv << 6) | ln; }
;     ...
;         const float l0 = lsum[0] + __shfl_xor(lsum[0], 32), l1 = lsum[1] + __shfl_xor(lsum[1], 32);
;         const float i0 = 1.0f / l0, i1 = lam / l1;
;         float ss = 0.f;
; #pragma unroll
;         for (int d = 0; d < 2; ++d)
; #pragma unroll
;             for (int r = 0; r < 16; ++r) { const float o = O[0][d][r] * i0 - O[1][d][r] * i1; O[0][d][r] = o; ss += o * o; }
;         ss += __shfl_xor(ss, 32);
;         const float rn = frsq(ss * (1.f / 64.f) + 1e-5f) * (1.0f - lam_init);
;         const int lane2 = lt_tid(wvid) & 63, qpos2 = q0w + (lane2 & 31), hi2 = lane2 >> 5;
;         if (wave_on && qpos2 < LT && (qi > 0 || qpos2 < NMETA)) {
.LBB0_793:
	ds_bpermute_b32 v0, v190, v191
	ds_bpermute_b32 v66, v190, v192
	s_and_b64 s[0:1], s[24:25], exec
	s_waitcnt lgkmcnt(1)
	v_add_f32_e32 v0, v191, v0
	v_div_scale_f32 v67, s[0:1], v0, v0, 1.0
	v_rcp_f32_e32 v68, v67
	s_waitcnt lgkmcnt(0)
	v_add_f32_e32 v66, v192, v66
	v_fma_f32 v69, -v67, v68, 1.0
	v_fmac_f32_e32 v68, v69, v68
	v_div_scale_f32 v69, vcc, 1.0, v0, 1.0
	v_mul_f32_e32 v70, v69, v68
	v_fma_f32 v71, -v67, v70, v69
	v_fmac_f32_e32 v70, v71, v68
	v_fma_f32 v67, -v67, v70, v69
	v_div_fmas_f32 v67, v67, v68, v70
	v_div_fixup_f32 v0, v67, v0, 1.0
	v_div_scale_f32 v67, s[0:1], v66, v66, v184
	v_rcp_f32_e32 v68, v67
	s_cselect_b32 s0, 0x1010, 16
	v_fma_f32 v69, -v67, v68, 1.0
	v_fmac_f32_e32 v68, v69, v68
	v_div_scale_f32 v69, vcc, v184, v66, v184
	v_mul_f32_e32 v70, v69, v68
	v_fma_f32 v71, -v67, v70, v69
	v_fmac_f32_e32 v70, v71, v68
	v_fma_f32 v67, -v67, v70, v69
	v_div_fmas_f32 v67, v67, v68, v70
	v_div_fixup_f32 v70, v67, v66, v184
	v_pk_mul_f32 v[34:35], v[34:35], v[70:71] op_sel_hi:[1,0]
	v_pk_mul_f32 v[2:3], v[2:3], v[70:71] op_sel_hi:[1,0]
	v_pk_fma_f32 v[66:67], v[50:51], v[0:1], v[34:35] op_sel_hi:[1,0,1] neg_lo:[0,0,1] neg_hi:[0,0,1]
	v_pk_mul_f32 v[34:35], v[36:37], v[70:71] op_sel_hi:[1,0]
	v_pk_fma_f32 v[36:37], v[18:19], v[0:1], v[2:3] op_sel_hi:[1,0,1] neg_lo:[0,0,1] neg_hi:[0,0,1]
	v_pk_fma_f32 v[68:69], v[52:53], v[0:1], v[34:35] op_sel_hi:[1,0,1] neg_lo:[0,0,1] neg_hi:[0,0,1]
	v_pk_mul_f32 v[34:35], v[38:39], v[70:71] op_sel_hi:[1,0]
	v_pk_mul_f32 v[2:3], v[4:5], v[70:71] op_sel_hi:[1,0]
	v_pk_fma_f32 v[54:55], v[54:55], v[0:1], v[34:35] op_sel_hi:[1,0,1] neg_lo:[0,0,1] neg_hi:[0,0,1]
	v_pk_mul_f32 v[34:35], v[40:41], v[70:71] op_sel_hi:[1,0]
	v_pk_mul_f32 v[72:73], v[66:67], v[66:67]
	v_pk_fma_f32 v[52:53], v[56:57], v[0:1], v[34:35] op_sel_hi:[1,0,1] neg_lo:[0,0,1] neg_hi:[0,0,1]
	v_pk_mul_f32 v[34:35], v[42:43], v[70:71] op_sel_hi:[1,0]
	v_pk_mul_f32 v[74:75], v[68:69], v[68:69]
	v_pk_fma_f32 v[50:51], v[58:59], v[0:1], v[34:35] op_sel_hi:[1,0,1] neg_lo:[0,0,1] neg_hi:[0,0,1]
	v_pk_mul_f32 v[34:35], v[44:45], v[70:71] op_sel_hi:[1,0]
	v_pk_mul_f32 v[76:77], v[54:55], v[54:55]
	v_pk_fma_f32 v[42:43], v[60:61], v[0:1], v[34:35] op_sel_hi:[1,0,1] neg_lo:[0,0,1] neg_hi:[0,0,1]
	v_pk_mul_f32 v[34:35], v[46:47], v[70:71] op_sel_hi:[1,0]
	v_pk_mul_f32 v[56:57], v[52:53], v[52:53]
	v_pk_fma_f32 v[40:41], v[62:63], v[0:1], v[34:35] op_sel_hi:[1,0,1] neg_lo:[0,0,1] neg_hi:[0,0,1]
	v_pk_mul_f32 v[34:35], v[48:49], v[70:71] op_sel_hi:[1,0]
	v_pk_mul_f32 v[58:59], v[50:51], v[50:51]
	v_pk_fma_f32 v[38:39], v[64:65], v[0:1], v[34:35] op_sel_hi:[1,0,1] neg_lo:[0,0,1] neg_hi:[0,0,1]
	v_pk_fma_f32 v[34:35], v[20:21], v[0:1], v[2:3] op_sel_hi:[1,0,1] neg_lo:[0,0,1] neg_hi:[0,0,1]
	v_pk_mul_f32 v[2:3], v[6:7], v[70:71] op_sel_hi:[1,0]
	v_pk_mul_f32 v[44:45], v[42:43], v[42:43]
	v_pk_fma_f32 v[20:21], v[22:23], v[0:1], v[2:3] op_sel_hi:[1,0,1] neg_lo:[0,0,1] neg_hi:[0,0,1]
	v_pk_mul_f32 v[2:3], v[8:9], v[70:71] op_sel_hi:[1,0]
	v_pk_mul_f32 v[46:47], v[40:41], v[40:41]
	v_pk_fma_f32 v[18:19], v[24:25], v[0:1], v[2:3] op_sel_hi:[1,0,1] neg_lo:[0,0,1] neg_hi:[0,0,1]
	v_pk_mul_f32 v[2:3], v[10:11], v[70:71] op_sel_hi:[1,0]
	v_pk_mul_f32 v[48:49], v[38:39], v[38:39]
	v_pk_fma_f32 v[8:9], v[26:27], v[0:1], v[2:3] op_sel_hi:[1,0,1] neg_lo:[0,0,1] neg_hi:[0,0,1]
	v_pk_mul_f32 v[2:3], v[12:13], v[70:71] op_sel_hi:[1,0]
	v_pk_mul_f32 v[60:61], v[36:37], v[36:37]
	v_pk_fma_f32 v[6:7], v[28:29], v[0:1], v[2:3] op_sel_hi:[1,0,1] neg_lo:[0,0,1] neg_hi:[0,0,1]
	v_pk_mul_f32 v[2:3], v[14:15], v[70:71] op_sel_hi:[1,0]
	v_pk_mul_f32 v[62:63], v[34:35], v[34:35]
	v_pk_fma_f32 v[4:5], v[30:31], v[0:1], v[2:3] op_sel_hi:[1,0,1] neg_lo:[0,0,1] neg_hi:[0,0,1]
	v_pk_mul_f32 v[2:3], v[16:17], v[70:71] op_sel_hi:[1,0]
	v_pk_mul_f32 v[22:23], v[20:21], v[20:21]
	v_pk_fma_f32 v[2:3], v[32:33], v[0:1], v[2:3] op_sel_hi:[1,0,1] neg_lo:[0,0,1] neg_hi:[0,0,1]
	v_add_f32_e32 v0, v72, v73
	v_add_f32_e32 v0, v74, v0
	v_add_f32_e32 v0, v75, v0
	v_add_f32_e32 v0, v76, v0
	v_add_f32_e32 v0, v77, v0
	v_add_f32_e32 v0, v56, v0
	v_add_f32_e32 v0, v57, v0
	v_add_f32_e32 v0, v58, v0
	v_add_f32_e32 v0, v59, v0
	v_add_f32_e32 v0, v44, v0
	v_add_f32_e32 v0, v45, v0
	v_add_f32_e32 v0, v46, v0
	v_add_f32_e32 v0, v47, v0
	v_add_f32_e32 v0, v48, v0
	v_add_f32_e32 v0, v49, v0
	v_add_f32_e32 v0, v60, v0
	v_add_f32_e32 v0, v61, v0
	v_add_f32_e32 v0, v62, v0
	v_add_f32_e32 v0, v63, v0
	v_add_f32_e32 v0, v22, v0
	v_pk_mul_f32 v[24:25], v[18:19], v[18:19]
	v_add_f32_e32 v0, v23, v0
	v_add_f32_e32 v0, v24, v0
	v_pk_mul_f32 v[10:11], v[8:9], v[8:9]
	v_add_f32_e32 v0, v25, v0
	v_add_f32_e32 v0, v10, v0
	v_pk_mul_f32 v[12:13], v[6:7], v[6:7]
	v_add_f32_e32 v0, v11, v0
	v_add_f32_e32 v0, v12, v0
	v_pk_mul_f32 v[14:15], v[4:5], v[4:5]
	v_add_f32_e32 v0, v13, v0
	v_add_f32_e32 v0, v14, v0
	v_pk_mul_f32 v[16:17], v[2:3], v[2:3]
	v_add_f32_e32 v0, v15, v0
	v_add_f32_e32 v0, v16, v0
	v_add_f32_e32 v10, v17, v0
	ds_bpermute_b32 v11, v190, v10
	v_mbcnt_lo_u32_b32 v0, -1, 0
	v_mbcnt_hi_u32_b32 v0, -1, v0
	s_nop 0
	v_and_b32_e32 v12, 31, v0
	v_add_u32_e32 v12, s49, v12
	v_cmp_gt_i32_e32 vcc, s0, v12
	s_and_b64 s[0:1], s[28:29], vcc
	s_and_saveexec_b64 s[24:25], s[0:1]
	s_xor_b64 s[0:1], exec, s[24:25]
	s_cbranch_execz .LBB0_768
; __device__ __forceinline__ float frsq(float x) { return __builtin_amdgcn_rsqf(x); }
; __device__ __forceinline__ int lt_tid(int wv) { int ln; asm volatile("v_mbcnt_lo_u32_b32 %0, -1, 0\n\tv_mbcnt_hi_u32_b32 %0, -1, %0" : "=v"(ln)); return (wv << 6) | ln; }
; __device__ __forceinline__ unsigned pkbf(float lo, float hi) { f32x2_t v = {lo, hi}; bf16x2_t b = __builtin_convertvector(v, bf16x2_t); return __builtin_bit_cast(unsigned, b); }
;     ...
;         const float rn = frsq(ss * (1.f / 64.f) + 1e-5f) * (1.0f - lam_init);
;         const int lane2 = lt_tid(wvid) & 63, qpos2 = q0w + (lane2 & 31), hi2 = lane2 >> 5;
;         if (wave_on && qpos2 < LT && (qi > 0 || qpos2 < NMETA)) {
;             bf16_t* orow = MIX + ((size_t)b * LT + qpos2) * D + M_B + h * 64;
; #pragma unroll
;             for (int d = 0; d < 2; ++d)
; #pragma unroll
;                 for (int g4 = 0; g4 < 4; ++g4) { const int dv0 = 32 * d + 8 * g4 + 4 * hi2; const f32x4 gg = *(const f32x4*)(p.in[I_SUBLN] + l * 64 + dv0);
;                     u32x2 w; w.x = pkbf(O[0][d][4 * g4] * rn * gg[0], O[0][d][4 * g4 + 1] * rn * gg[1]); w.y = pkbf(O[0][d][4 * g4 + 2] * rn * gg[2], O[0][d][4 * g4 + 3] * rn * gg[3]);
;                     *(u32x2*)(orow + dv0) = w; }
;         }
	v_ashrrev_i32_e32 v13, 31, v12
	v_lshl_add_u64 v[12:13], v[12:13], 0, s[22:23]
	v_lshrrev_b32_e32 v0, 3, v0
	v_lshlrev_b64 v[12:13], 11, v[12:13]
	v_and_b32_e32 v0, 4, v0
	s_waitcnt lgkmcnt(0)
	v_add_f32_e32 v10, v10, v11
	v_lshl_add_u64 v[12:13], s[6:7], 0, v[12:13]
	v_lshlrev_b32_e32 v11, 2, v0
	v_lshl_add_u64 v[16:17], v[12:13], 0, s[40:41]
	global_load_dwordx4 v[12:15], v11, s[20:21]
	global_load_dwordx4 v[114:117], v11, s[20:21] offset:32
	global_load_dwordx4 v[118:121], v11, s[20:21] offset:64
	global_load_dwordx4 v[122:125], v11, s[20:21] offset:96
	global_load_dwordx4 v[126:129], v11, s[20:21] offset:128
	global_load_dwordx4 v[130:133], v11, s[20:21] offset:160
	global_load_dwordx4 v[134:137], v11, s[20:21] offset:192
	global_load_dwordx4 v[138:141], v11, s[20:21] offset:224
	v_fmamk_f32 v10, v10, 0x3c800000, v204
	v_rsq_f32_e32 v10, v10
	v_lshlrev_b32_e32 v0, 1, v0
	s_mov_b64 s[22:23], 0xf1f0200
	v_mul_f32_e32 v10, v187, v10
	v_pk_mul_f32 v[22:23], v[66:67], v[10:11] op_sel_hi:[1,0]
	v_pk_mul_f32 v[20:21], v[20:21], v[10:11] op_sel_hi:[1,0]
	v_pk_mul_f32 v[18:19], v[18:19], v[10:11] op_sel_hi:[1,0]
	v_pk_mul_f32 v[8:9], v[8:9], v[10:11] op_sel_hi:[1,0]
	v_pk_mul_f32 v[6:7], v[6:7], v[10:11] op_sel_hi:[1,0]
	v_pk_mul_f32 v[4:5], v[4:5], v[10:11] op_sel_hi:[1,0]
	v_pk_mul_f32 v[2:3], v[2:3], v[10:11] op_sel_hi:[1,0]
	s_waitcnt vmcnt(0)
	v_pk_mul_f32 v[12:13], v[22:23], v[12:13]
	s_nop 0
	v_cvt_pk_bf16_f32 v22, v12, v13
	v_pk_mul_f32 v[12:13], v[68:69], v[10:11] op_sel_hi:[1,0]
	s_nop 0
	v_pk_mul_f32 v[12:13], v[12:13], v[14:15]
	v_lshl_add_u64 v[14:15], v[16:17], 0, v[0:1]
	v_cvt_pk_bf16_f32 v23, v12, v13
	v_lshl_add_u64 v[12:13], v[14:15], 0, s[22:23]
	s_mov_b32 s22, 0xf1f0000
	v_add_co_u32_e32 v14, vcc, s22, v14
	s_nop 1
	v_addc_co_u32_e32 v15, vcc, 0, v15, vcc
	global_store_dwordx2 v[14:15], v[22:23], off offset:512
	s_nop 1
	v_mov_b64_e32 v[14:15], v[114:115]
	v_mov_b64_e32 v[16:17], v[116:117]
	v_pk_mul_f32 v[22:23], v[54:55], v[10:11] op_sel_hi:[1,0]
	v_pk_mul_f32 v[14:15], v[22:23], v[14:15]
	v_pk_mul_f32 v[22:23], v[52:53], v[10:11] op_sel_hi:[1,0]
	v_cvt_pk_bf16_f32 v14, v14, v15
	v_pk_mul_f32 v[16:17], v[22:23], v[16:17]
	v_pk_mul_f32 v[22:23], v[50:51], v[10:11] op_sel_hi:[1,0]
	v_cvt_pk_bf16_f32 v15, v16, v17
	global_store_dwordx2 v[12:13], v[14:15], off offset:16
	s_nop 1
	v_mov_b64_e32 v[14:15], v[118:119]
	v_mov_b64_e32 v[16:17], v[120:121]
	v_pk_mul_f32 v[14:15], v[22:23], v[14:15]
	v_pk_mul_f32 v[22:23], v[42:43], v[10:11] op_sel_hi:[1,0]
	v_cvt_pk_bf16_f32 v14, v14, v15
	v_pk_mul_f32 v[16:17], v[22:23], v[16:17]
	v_pk_mul_f32 v[22:23], v[40:41], v[10:11] op_sel_hi:[1,0]
	v_cvt_pk_bf16_f32 v15, v16, v17
	global_store_dwordx2 v[12:13], v[14:15], off offset:32
	s_nop 1
	v_mov_b64_e32 v[14:15], v[122:123]
	v_mov_b64_e32 v[16:17], v[124:125]
	v_pk_mul_f32 v[14:15], v[22:23], v[14:15]
	v_pk_mul_f32 v[22:23], v[38:39], v[10:11] op_sel_hi:[1,0]
	v_cvt_pk_bf16_f32 v14, v14, v15
	v_pk_mul_f32 v[16:17], v[22:23], v[16:17]
	v_pk_mul_f32 v[22:23], v[36:37], v[10:11] op_sel_hi:[1,0]
	v_cvt_pk_bf16_f32 v15, v16, v17
	global_store_dwordx2 v[12:13], v[14:15], off offset:48
	s_nop 1
	v_mov_b64_e32 v[14:15], v[126:127]
	v_mov_b64_e32 v[16:17], v[128:129]
	v_pk_mul_f32 v[14:15], v[22:23], v[14:15]
	v_pk_mul_f32 v[22:23], v[34:35], v[10:11] op_sel_hi:[1,0]
	v_cvt_pk_bf16_f32 v14, v14, v15
	v_pk_mul_f32 v[16:17], v[22:23], v[16:17]
	s_nop 0
	v_cvt_pk_bf16_f32 v15, v16, v17
	global_store_dwordx2 v[12:13], v[14:15], off offset:64
	s_nop 1
	v_mov_b64_e32 v[14:15], v[130:131]
	v_mov_b64_e32 v[16:17], v[132:133]
	v_pk_mul_f32 v[14:15], v[20:21], v[14:15]
	v_pk_mul_f32 v[16:17], v[18:19], v[16:17]
	v_cvt_pk_bf16_f32 v14, v14, v15
	v_cvt_pk_bf16_f32 v15, v16, v17
	global_store_dwordx2 v[12:13], v[14:15], off offset:80
	s_nop 1
	v_mov_b64_e32 v[14:15], v[134:135]
	v_mov_b64_e32 v[16:17], v[136:137]
	v_pk_mul_f32 v[8:9], v[8:9], v[14:15]
	v_pk_mul_f32 v[6:7], v[6:7], v[16:17]
	v_cvt_pk_bf16_f32 v8, v8, v9
	v_cvt_pk_bf16_f32 v9, v6, v7
	global_store_dwordx2 v[12:13], v[8:9], off offset:96
	s_nop 1
	v_mov_b64_e32 v[6:7], v[138:139]
	v_mov_b64_e32 v[8:9], v[140:141]
	v_pk_mul_f32 v[4:5], v[4:5], v[6:7]
	v_pk_mul_f32 v[2:3], v[2:3], v[8:9]
	v_cvt_pk_bf16_f32 v4, v4, v5
	v_cvt_pk_bf16_f32 v5, v2, v3
	global_store_dwordx2 v[12:13], v[4:5], off offset:112
	s_branch .LBB0_768

;     ...
;     if (tid < 4) { float bx = -1e30f; for (int n = 0; n < 32; ++n) bx = fmaxf(bx, p.in[I_RELB][n * 8 + tid]); btab[tid * 132 + 131] = bx * LOG2E; }
.LBB0_802:
	s_or_b64 exec, exec, s[2:3]
	v_cmp_gt_i32_e32 vcc, 4, v2
	s_and_saveexec_b64 s[2:3], vcc
	s_cbranch_execz .LBB0_804
	v_readlane_b32 s48, v253, 12
	v_ashrrev_i32_e32 v3, 31, v2
	v_readlane_b32 s60, v253, 24
	v_readlane_b32 s61, v253, 25
	s_mov_b32 s4, 0xf149f2ca
	v_readlane_b32 s49, v253, 13
	v_lshl_add_u64 v[4:5], v[2:3], 2, s[60:61]
	global_load_dword v0, v[4:5], off
	global_load_dword v3, v[4:5], off offset:32
	global_load_dword v8, v[4:5], off offset:64
	global_load_dword v9, v[4:5], off offset:96
	global_load_dword v10, v[4:5], off offset:128
	global_load_dword v11, v[4:5], off offset:160
	global_load_dword v12, v[4:5], off offset:192
	global_load_dword v13, v[4:5], off offset:224
	global_load_dword v14, v[4:5], off offset:256
	global_load_dword v15, v[4:5], off offset:288
	global_load_dword v16, v[4:5], off offset:320
	global_load_dword v17, v[4:5], off offset:352
	global_load_dword v18, v[4:5], off offset:384
	global_load_dword v19, v[4:5], off offset:416
	global_load_dword v20, v[4:5], off offset:448
	global_load_dword v21, v[4:5], off offset:480
	global_load_dword v22, v[4:5], off offset:512
	global_load_dword v23, v[4:5], off offset:544
	global_load_dword v24, v[4:5], off offset:576
	global_load_dword v25, v[4:5], off offset:608
	global_load_dword v26, v[4:5], off offset:640
	global_load_dword v27, v[4:5], off offset:672
	global_load_dword v28, v[4:5], off offset:704
	global_load_dword v29, v[4:5], off offset:736
	global_load_dword v30, v[4:5], off offset:768
	global_load_dword v31, v[4:5], off offset:800
	global_load_dword v32, v[4:5], off offset:832
	global_load_dword v33, v[4:5], off offset:864
	global_load_dword v34, v[4:5], off offset:896
	global_load_dword v35, v[4:5], off offset:928
	global_load_dword v36, v[4:5], off offset:960
	global_load_dword v37, v[4:5], off offset:992
	v_readlane_b32 s50, v253, 14
	v_readlane_b32 s51, v253, 15
	v_readlane_b32 s52, v253, 16
	v_readlane_b32 s53, v253, 17
	v_readlane_b32 s54, v253, 18
	v_readlane_b32 s55, v253, 19
	v_readlane_b32 s56, v253, 20
	v_readlane_b32 s57, v253, 21
	v_readlane_b32 s58, v253, 22
	v_readlane_b32 s59, v253, 23
	v_readlane_b32 s62, v253, 26
	v_readlane_b32 s63, v253, 27
	s_waitcnt vmcnt(0)
	v_max3_f32 v0, v0, s4, v3
	v_mov_b32_e32 v3, v8
	v_mov_b32_e32 v7, v9
	s_movk_i32 s4, 0x210
	s_waitcnt vmcnt(0)
	v_max3_f32 v0, v0, v3, v7
	v_mov_b32_e32 v3, v10
	v_mov_b32_e32 v7, v11
	s_waitcnt vmcnt(0)
	v_max3_f32 v0, v0, v3, v7
	v_mov_b32_e32 v3, v12
	v_mov_b32_e32 v7, v13
	s_waitcnt vmcnt(0)
	v_max3_f32 v0, v0, v3, v7
	v_mov_b32_e32 v3, v14
	v_mov_b32_e32 v7, v15
	s_waitcnt vmcnt(0)
	v_max3_f32 v0, v0, v3, v7
	v_mov_b32_e32 v3, v16
	v_mov_b32_e32 v7, v17
	s_waitcnt vmcnt(0)
	v_max3_f32 v0, v0, v3, v7
	v_mov_b32_e32 v3, v18
	v_mov_b32_e32 v7, v19
	s_waitcnt vmcnt(0)
	v_max3_f32 v0, v0, v3, v7
	v_mov_b32_e32 v3, v20
	v_mov_b32_e32 v7, v21
	s_waitcnt vmcnt(0)
	v_max3_f32 v0, v0, v3, v7
	v_mov_b32_e32 v3, v22
	v_mov_b32_e32 v7, v23
	s_waitcnt vmcnt(0)
	v_max3_f32 v0, v0, v3, v7
	v_mov_b32_e32 v3, v24
	v_mov_b32_e32 v7, v25
	s_waitcnt vmcnt(0)
	v_max3_f32 v0, v0, v3, v7
	v_mov_b32_e32 v3, v26
	v_mov_b32_e32 v7, v27
	s_waitcnt vmcnt(0)
	v_max3_f32 v0, v0, v3, v7
	v_mov_b32_e32 v3, v28
	v_mov_b32_e32 v7, v29
	s_waitcnt vmcnt(0)
	v_max3_f32 v0, v0, v3, v7
	v_mov_b32_e32 v3, v30
	v_mov_b32_e32 v7, v31
	s_waitcnt vmcnt(0)
	v_max3_f32 v0, v0, v3, v7
	v_mov_b32_e32 v3, v32
	v_mov_b32_e32 v7, v33
	s_waitcnt vmcnt(0)
	v_max3_f32 v0, v0, v3, v7
	v_mov_b32_e32 v3, v34
	v_mov_b32_e32 v7, v35
	s_waitcnt vmcnt(0)
	v_max3_f32 v0, v0, v3, v7
	v_mov_b32_e32 v3, v36
	s_nop 0
	v_mov_b32_e32 v4, v37
	s_waitcnt vmcnt(0)
	v_max3_f32 v0, v0, v3, v4
	v_mul_lo_u32 v3, v2, s4
	v_mul_f32_e32 v0, 0x3fb8aa3b, v0
	v_add_u32_e32 v3, 0, v3
	ds_write_b32 v3, v0 offset:524

; __device__ __forceinline__ float bflo(unsigned w) { return __uint_as_float(w << 16); }
; __device__ __forceinline__ float bfhi(unsigned w) { return __uint_as_float(w & 0xFFFF0000u); }
; __device__ __forceinline__ void ph_ln1(const Params& p, int l, LAS unsigned char* lds, const int wvid) {
;     ...
;     for (int r = gw; r < T; r += NGW, ++k) {
;         f32x4 v[4]; u32x2 zc[4];
; #pragma unroll
;         for (int j = 0; j < 4; ++j) { zc[j] = zn[j]; zn[j] = *(const u32x2*)(Z + (size_t)min(r + NGW, T - 1) * D + 4 * lane + 256 * j); }
;         if (r < MP - 256) {
; #pragma unroll
;             for (int j = 0; j < 4; ++j) { const u32x2 z = zc[j]; v[j] = (f32x4){bflo(z.x), bfhi(z.x), bflo(z.y), bfhi(z.y)}; }
;         } else {
;             const float* zp = (const float*)(ws + WS_ZP) + (size_t)(r - (MP - 256)) * D + 4 * lane;
; #pragma unroll
;             for (int j = 0; j < 4; ++j) { const u32x2 hh = *(const u32x2*)(HB + (size_t)r * D + 4 * lane + 256 * j); f32x4 a = (f32x4){ALPHA * bflo(hh.x), ALPHA * bfhi(hh.x), ALPHA * bflo(hh.y), ALPHA * bfhi(hh.y)};
; #pragma unroll
;                 for (int k2 = 0; k2 < ZSPLIT; ++k2) a = a + *(const f32x4*)(zp + (size_t)k2 * 256 * D + 256 * j);
;                 v[j] = a; }
;         }
.LBB0_1074:
	v_add_u32_e32 v87, s80, v34
	v_min_i32_e32 v36, 0x807f, v87
	v_ashrrev_i32_e32 v37, 31, v36
	v_lshlrev_b64 v[36:37], 11, v[36:37]
	v_lshl_add_u64 v[36:37], v[44:45], 0, v[36:37]
	s_waitcnt vmcnt(3)
	v_mov_b64_e32 v[64:65], v[56:57]
	s_waitcnt vmcnt(2)
	v_mov_b64_e32 v[70:71], v[54:55]
	s_waitcnt vmcnt(1)
	v_mov_b64_e32 v[80:81], v[52:53]
	s_waitcnt vmcnt(0)
	v_mov_b64_e32 v[82:83], v[50:51]
	global_load_dwordx2 v[50:51], v[36:37], off
	global_load_dwordx2 v[52:53], v[36:37], off offset:512
	global_load_dwordx2 v[54:55], v[36:37], off offset:1024
	global_load_dwordx2 v[56:57], v[36:37], off offset:1536
	v_cmp_lt_i32_e64 s[0:1], s79, v34
	s_and_saveexec_b64 s[22:23], s[0:1]
	s_xor_b64 s[22:23], exec, s[22:23]
	s_cbranch_execz .LBB0_1076
	v_mov_b32_e32 v35, v1
	v_add_u32_e32 v0, 0xffff8000, v34
	v_lshlrev_b64 v[34:35], 11, v[34:35]
	v_lshl_add_u64 v[76:77], v[46:47], 0, v[34:35]
	global_load_dwordx2 v[34:35], v[76:77], off
	v_lshlrev_b64 v[36:37], 12, v[0:1]
	v_lshl_add_u64 v[74:75], v[48:49], 0, v[36:37]
	s_mov_b32 s0, 0x100000
	v_add_co_u32_e64 v184, s[0:1], s0, v74
	s_nop 1
	v_addc_co_u32_e64 v185, s[0:1], 0, v75, s[0:1]
	s_mov_b32 s0, 0x200000
	s_nop 0
	v_add_co_u32_e64 v186, s[0:1], s0, v74
	s_nop 1
	v_addc_co_u32_e64 v187, s[0:1], 0, v75, s[0:1]
	s_mov_b32 s0, 0x300000
	s_nop 0
	v_add_co_u32_e64 v188, s[0:1], s0, v74
	s_nop 1
	v_addc_co_u32_e64 v189, s[0:1], 0, v75, s[0:1]
	global_load_dwordx4 v[118:121], v[74:75], off
	global_load_dwordx4 v[122:125], v[184:185], off
	global_load_dwordx4 v[126:129], v[186:187], off
	global_load_dwordx4 v[130:133], v[188:189], off
	global_load_dwordx2 v[88:89], v[76:77], off offset:512
	global_load_dwordx4 v[134:137], v[74:75], off offset:1024
	global_load_dwordx4 v[138:141], v[184:185], off offset:1024
	global_load_dwordx4 v[142:145], v[186:187], off offset:1024
	global_load_dwordx4 v[146:149], v[188:189], off offset:1024
	global_load_dwordx2 v[90:91], v[76:77], off offset:1024
	global_load_dwordx2 v[92:93], v[76:77], off offset:1536
	global_load_dwordx4 v[232:235], v[74:75], off offset:2048
	global_load_dwordx4 v[236:239], v[184:185], off offset:2048
	global_load_dwordx4 v[240:243], v[186:187], off offset:2048
	global_load_dwordx4 v[244:247], v[188:189], off offset:2048
	global_load_dwordx4 v[196:199], v[74:75], off offset:3072
	global_load_dwordx4 v[200:203], v[184:185], off offset:3072
	global_load_dwordx4 v[206:209], v[186:187], off offset:3072
	global_load_dwordx4 v[210:213], v[188:189], off offset:3072
	s_mov_b32 s0, 0x100000
	v_add_co_u32_e64 v72, s[0:1], s0, v74
	s_waitcnt vmcnt(0)
	v_lshlrev_b32_e32 v60, 16, v34
	v_and_b32_e32 v61, 0xffff0000, v34
	v_lshlrev_b32_e32 v62, 16, v35
	v_and_b32_e32 v63, 0xffff0000, v35
	v_mov_b64_e32 v[34:35], v[118:119]
	v_mov_b64_e32 v[36:37], v[120:121]
	v_addc_co_u32_e64 v73, s[0:1], 0, v75, s[0:1]
	s_mov_b32 s0, 0x200000
	s_nop 0
	v_add_co_u32_e64 v70, s[0:1], s0, v74
	s_waitcnt vmcnt(0)
	v_pk_fma_f32 v[60:61], v[60:61], s[88:89], v[34:35] op_sel_hi:[1,0,1]
	v_pk_fma_f32 v[62:63], v[62:63], s[88:89], v[36:37] op_sel_hi:[1,0,1]
	v_mov_b64_e32 v[34:35], v[122:123]
	v_mov_b64_e32 v[36:37], v[124:125]
	v_addc_co_u32_e64 v71, s[0:1], 0, v75, s[0:1]
	s_mov_b32 s0, 0x300000
	s_nop 0
	v_add_co_u32_e64 v68, s[0:1], s0, v74
	s_waitcnt vmcnt(0)
	v_pk_add_f32 v[62:63], v[36:37], v[62:63]
	v_pk_add_f32 v[60:61], v[34:35], v[60:61]
	v_mov_b64_e32 v[34:35], v[126:127]
	v_mov_b64_e32 v[36:37], v[128:129]
	v_addc_co_u32_e64 v69, s[0:1], 0, v75, s[0:1]
	s_waitcnt vmcnt(0)
	v_pk_add_f32 v[36:37], v[36:37], v[62:63]
	v_pk_add_f32 v[64:65], v[34:35], v[60:61]
	v_mov_b64_e32 v[60:61], v[130:131]
	v_mov_b64_e32 v[62:63], v[132:133]
	s_waitcnt vmcnt(0)
	v_pk_add_f32 v[34:35], v[62:63], v[36:37]
	v_mov_b64_e32 v[36:37], v[88:89]
	v_pk_add_f32 v[64:65], v[60:61], v[64:65]
	v_mov_b64_e32 v[60:61], v[134:135]
	v_mov_b64_e32 v[62:63], v[136:137]
	s_waitcnt vmcnt(1)
	v_lshlrev_b32_e32 v66, 16, v36
	v_and_b32_e32 v67, 0xffff0000, v36
	v_lshlrev_b32_e32 v36, 16, v37
	v_and_b32_e32 v37, 0xffff0000, v37
	s_waitcnt vmcnt(0)
	v_pk_fma_f32 v[66:67], v[66:67], s[88:89], v[60:61] op_sel_hi:[1,0,1]
	v_pk_fma_f32 v[36:37], v[36:37], s[88:89], v[62:63] op_sel_hi:[1,0,1]
	v_mov_b64_e32 v[60:61], v[138:139]
	v_mov_b64_e32 v[62:63], v[140:141]
	s_waitcnt vmcnt(0)
	v_pk_add_f32 v[36:37], v[62:63], v[36:37]
	v_pk_add_f32 v[66:67], v[60:61], v[66:67]
	v_mov_b64_e32 v[60:61], v[142:143]
	v_mov_b64_e32 v[62:63], v[144:145]
	s_waitcnt vmcnt(0)
	v_pk_add_f32 v[36:37], v[62:63], v[36:37]
	v_pk_add_f32 v[66:67], v[60:61], v[66:67]
	v_mov_b64_e32 v[60:61], v[146:147]
	v_mov_b64_e32 v[62:63], v[148:149]
	s_waitcnt vmcnt(0)
	v_pk_add_f32 v[66:67], v[60:61], v[66:67]
	v_mov_b64_e32 v[60:61], v[90:91]
	v_pk_add_f32 v[36:37], v[62:63], v[36:37]
	v_mov_b64_e32 v[76:77], v[92:93]
	s_waitcnt vmcnt(1)
	v_lshlrev_b32_e32 v78, 16, v60
	v_and_b32_e32 v79, 0xffff0000, v60
	v_lshlrev_b32_e32 v80, 16, v61
	v_and_b32_e32 v81, 0xffff0000, v61
	v_mov_b64_e32 v[60:61], v[232:233]
	v_mov_b64_e32 v[62:63], v[234:235]
	s_waitcnt vmcnt(0)
	v_pk_fma_f32 v[78:79], v[78:79], s[88:89], v[60:61] op_sel_hi:[1,0,1]
	v_pk_fma_f32 v[80:81], v[80:81], s[88:89], v[62:63] op_sel_hi:[1,0,1]
	v_mov_b64_e32 v[60:61], v[236:237]
	v_mov_b64_e32 v[62:63], v[238:239]
	s_waitcnt vmcnt(0)
	v_pk_add_f32 v[80:81], v[62:63], v[80:81]
	v_pk_add_f32 v[78:79], v[60:61], v[78:79]
	v_mov_b64_e32 v[60:61], v[240:241]
	v_mov_b64_e32 v[62:63], v[242:243]
	s_waitcnt vmcnt(0)
	v_pk_add_f32 v[62:63], v[62:63], v[80:81]
	v_pk_add_f32 v[82:83], v[60:61], v[78:79]
	v_mov_b64_e32 v[78:79], v[244:245]
	v_mov_b64_e32 v[80:81], v[246:247]
	s_waitcnt vmcnt(0)
	v_pk_add_f32 v[60:61], v[80:81], v[62:63]
	v_pk_add_f32 v[62:63], v[78:79], v[82:83]
	v_lshlrev_b32_e32 v78, 16, v76
	v_and_b32_e32 v79, 0xffff0000, v76
	v_lshlrev_b32_e32 v80, 16, v77
	v_and_b32_e32 v81, 0xffff0000, v77
	v_mov_b64_e32 v[74:75], v[196:197]
	v_mov_b64_e32 v[76:77], v[198:199]
	s_waitcnt vmcnt(0)
	v_pk_fma_f32 v[78:79], v[78:79], s[88:89], v[74:75] op_sel_hi:[1,0,1]
	v_mov_b64_e32 v[72:73], v[200:201]
	v_mov_b64_e32 v[74:75], v[202:203]
	v_pk_fma_f32 v[76:77], v[80:81], s[88:89], v[76:77] op_sel_hi:[1,0,1]
	s_waitcnt vmcnt(0)
	v_pk_add_f32 v[74:75], v[74:75], v[76:77]
	v_pk_add_f32 v[76:77], v[72:73], v[78:79]
	v_mov_b64_e32 v[70:71], v[206:207]
	v_mov_b64_e32 v[72:73], v[208:209]
	s_waitcnt vmcnt(0)
	v_pk_add_f32 v[72:73], v[72:73], v[74:75]
	v_pk_add_f32 v[74:75], v[70:71], v[76:77]
	v_mov_b64_e32 v[68:69], v[210:211]
	v_mov_b64_e32 v[70:71], v[212:213]
	s_waitcnt vmcnt(0)
	v_pk_add_f32 v[72:73], v[70:71], v[72:73]
	v_pk_add_f32 v[74:75], v[68:69], v[74:75]
	v_mov_b32_e32 v76, v73
	v_mov_b32_e32 v78, v75
	v_mov_b32_e32 v69, v36
	v_mov_b32_e32 v68, v67
	v_mov_b32_e32 v36, v66
	v_mov_b32_e32 v67, v34
	v_mov_b32_e32 v66, v65
	v_mov_b32_e32 v34, v64

; __device__ __forceinline__ unsigned cvt_pk_bf16(float lo, float hi) { f32x2c v = {lo, hi}; bf16x2c b = __builtin_convertvector(v, bf16x2c); return __builtin_bit_cast(unsigned, b); }
;     __device__ __forceinline__ void operator()(const f32x4 (&acc)[2][2][4][2], const Unit& u, int wr, int wc, int fr, int fq) const {
;     ...
;             for (int m = 0; m < 4; ++m) { const int row = row0 + ai * HALF + m * 16; if (row < u.rend) { const float g = gt[ai][m]; bf16_t* rowp = Y + (size_t)row * D + col0;
; #pragma unroll
;                 for (int bj = 0; bj < 2; ++bj) { const f32x4 v0 = acc[ai][bj][m][0] * g, v1 = acc[ai][bj][m][1] * g;
;                     u32x4 w; w.x = cvt_pk_bf16(v0[0], v0[1]); w.y = cvt_pk_bf16(v0[2], v0[3]); w.z = cvt_pk_bf16(v1[0], v1[1]); w.w = cvt_pk_bf16(v1[2], v1[3]);
;                     *(u32x4*)(rowp + bj * HALF) = w; } } }
.LBB0_1490:
	v_ashrrev_i32_e32 v159, 31, v158
	v_lshlrev_b64 v[90:91], 11, v[158:159]
	v_lshl_add_u64 v[90:91], s[18:19], 0, v[90:91]
	v_lshl_add_u64 v[94:95], v[136:137], 1, v[90:91]
	s_waitcnt vmcnt(2)
	v_pk_mul_f32 v[92:93], v[120:121], v[156:157] op_sel_hi:[1,0]
	v_pk_mul_f32 v[90:91], v[118:119], v[156:157] op_sel_hi:[1,0]
	v_pk_mul_f32 v[96:97], v[116:117], v[156:157] op_sel_hi:[1,0]
	v_pk_mul_f32 v[114:115], v[114:115], v[156:157] op_sel_hi:[1,0]
	v_cvt_pk_bf16_f32 v90, v90, v91
	v_cvt_pk_bf16_f32 v91, v92, v93
	v_cvt_pk_bf16_f32 v92, v114, v115
	v_cvt_pk_bf16_f32 v93, v96, v97
	global_store_dwordx4 v[94:95], v[90:93], off
	v_pk_mul_f32 v[88:89], v[88:89], v[156:157] op_sel_hi:[1,0]
	v_pk_mul_f32 v[86:87], v[86:87], v[156:157] op_sel_hi:[1,0]
	v_pk_mul_f32 v[90:91], v[84:85], v[156:157] op_sel_hi:[1,0]
	v_pk_mul_f32 v[84:85], v[82:83], v[156:157] op_sel_hi:[1,0]
	v_cvt_pk_bf16_f32 v82, v86, v87
	v_cvt_pk_bf16_f32 v83, v88, v89
	v_cvt_pk_bf16_f32 v84, v84, v85
	v_cvt_pk_bf16_f32 v85, v90, v91
	global_store_dwordx4 v[94:95], v[82:85], off offset:256
	s_or_b64 exec, exec, s[0:1]
	v_cmp_lt_i32_e32 vcc, v154, v179
	s_and_saveexec_b64 s[0:1], vcc
	s_cbranch_execz .LBB0_1484
.LBB0_1491:
	v_ashrrev_i32_e32 v155, 31, v154
	v_lshlrev_b64 v[82:83], 11, v[154:155]
	v_lshl_add_u64 v[82:83], s[18:19], 0, v[82:83]
	v_lshl_add_u64 v[86:87], v[136:137], 1, v[82:83]
	s_waitcnt vmcnt(4)
	v_pk_mul_f32 v[84:85], v[112:113], v[152:153] op_sel_hi:[1,0]
	v_pk_mul_f32 v[82:83], v[110:111], v[152:153] op_sel_hi:[1,0]
	v_pk_mul_f32 v[88:89], v[108:109], v[152:153] op_sel_hi:[1,0]
	v_pk_mul_f32 v[90:91], v[106:107], v[152:153] op_sel_hi:[1,0]
	v_cvt_pk_bf16_f32 v82, v82, v83
	v_cvt_pk_bf16_f32 v83, v84, v85
	v_cvt_pk_bf16_f32 v84, v90, v91
	v_cvt_pk_bf16_f32 v85, v88, v89
	global_store_dwordx4 v[86:87], v[82:85], off
	v_pk_mul_f32 v[80:81], v[80:81], v[152:153] op_sel_hi:[1,0]
	v_pk_mul_f32 v[78:79], v[78:79], v[152:153] op_sel_hi:[1,0]
	v_pk_mul_f32 v[82:83], v[76:77], v[152:153] op_sel_hi:[1,0]
	v_pk_mul_f32 v[76:77], v[74:75], v[152:153] op_sel_hi:[1,0]
	v_cvt_pk_bf16_f32 v74, v78, v79
	v_cvt_pk_bf16_f32 v75, v80, v81
	v_cvt_pk_bf16_f32 v76, v76, v77
	v_cvt_pk_bf16_f32 v77, v82, v83
	global_store_dwordx4 v[86:87], v[74:77], off offset:256
	s_or_b64 exec, exec, s[0:1]
	v_cmp_lt_i32_e32 vcc, v150, v179
	s_and_saveexec_b64 s[0:1], vcc
	s_cbranch_execz .LBB0_1485
.LBB0_1492:
	v_ashrrev_i32_e32 v151, 31, v150
	v_lshlrev_b64 v[74:75], 11, v[150:151]
	v_lshl_add_u64 v[74:75], s[18:19], 0, v[74:75]
	v_lshl_add_u64 v[78:79], v[136:137], 1, v[74:75]
	s_waitcnt vmcnt(6)
	v_pk_mul_f32 v[76:77], v[104:105], v[148:149] op_sel_hi:[1,0]
	v_pk_mul_f32 v[74:75], v[102:103], v[148:149] op_sel_hi:[1,0]
	v_pk_mul_f32 v[80:81], v[100:101], v[148:149] op_sel_hi:[1,0]
	v_pk_mul_f32 v[82:83], v[98:99], v[148:149] op_sel_hi:[1,0]
	v_cvt_pk_bf16_f32 v74, v74, v75
	v_cvt_pk_bf16_f32 v75, v76, v77
	v_cvt_pk_bf16_f32 v76, v82, v83
	v_cvt_pk_bf16_f32 v77, v80, v81
	global_store_dwordx4 v[78:79], v[74:77], off
	v_pk_mul_f32 v[72:73], v[72:73], v[148:149] op_sel_hi:[1,0]
	v_pk_mul_f32 v[70:71], v[70:71], v[148:149] op_sel_hi:[1,0]
	v_pk_mul_f32 v[74:75], v[68:69], v[148:149] op_sel_hi:[1,0]
	v_pk_mul_f32 v[68:69], v[66:67], v[148:149] op_sel_hi:[1,0]
	v_cvt_pk_bf16_f32 v66, v70, v71
	v_cvt_pk_bf16_f32 v67, v72, v73
	v_cvt_pk_bf16_f32 v68, v68, v69
	v_cvt_pk_bf16_f32 v69, v74, v75
	global_store_dwordx4 v[78:79], v[66:69], off offset:256
	s_or_b64 exec, exec, s[0:1]
	v_cmp_lt_i32_e32 vcc, v146, v179
	s_and_saveexec_b64 s[0:1], vcc
	s_cbranch_execz .LBB0_1486
; __device__ __forceinline__ unsigned cvt_pk_bf16(float lo, float hi) { f32x2c v = {lo, hi}; bf16x2c b = __builtin_convertvector(v, bf16x2c); return __builtin_bit_cast(unsigned, b); }
;     __device__ __forceinline__ void operator()(const f32x4 (&acc)[2][2][4][2], const Unit& u, int wr, int wc, int fr, int fq) const {
;     ...
; #pragma unroll
;         for (int ai = 0; ai < 2; ++ai)
; #pragma unroll
;             for (int m = 0; m < 4; ++m) { const int row = row0 + ai * HALF + m * 16; if (row < u.rend) { const float g = gt[ai][m]; bf16_t* rowp = Y + (size_t)row * D + col0;
; #pragma unroll
;                 for (int bj = 0; bj < 2; ++bj) { const f32x4 v0 = acc[ai][bj][m][0] * g, v1 = acc[ai][bj][m][1] * g;
;                     u32x4 w; w.x = cvt_pk_bf16(v0[0], v0[1]); w.y = cvt_pk_bf16(v0[2], v0[3]); w.z = cvt_pk_bf16(v1[0], v1[1]); w.w = cvt_pk_bf16(v1[2], v1[3]);
;                     *(u32x4*)(rowp + bj * HALF) = w; } } }
.LBB0_1493:
	v_ashrrev_i32_e32 v147, 31, v146
	v_lshlrev_b64 v[66:67], 11, v[146:147]
	v_lshl_add_u64 v[66:67], s[18:19], 0, v[66:67]
	s_waitcnt vmcnt(8)
	v_pk_mul_f32 v[64:65], v[64:65], v[144:145] op_sel_hi:[1,0]
	v_pk_mul_f32 v[62:63], v[62:63], v[144:145] op_sel_hi:[1,0]
	v_pk_mul_f32 v[68:69], v[60:61], v[144:145] op_sel_hi:[1,0]
	v_pk_mul_f32 v[60:61], v[58:59], v[144:145] op_sel_hi:[1,0]
	v_lshl_add_u64 v[66:67], v[136:137], 1, v[66:67]
	v_cvt_pk_bf16_f32 v58, v62, v63
	v_cvt_pk_bf16_f32 v59, v64, v65
	v_cvt_pk_bf16_f32 v60, v60, v61
	v_cvt_pk_bf16_f32 v61, v68, v69
	global_store_dwordx4 v[66:67], v[58:61], off
	v_pk_mul_f32 v[56:57], v[56:57], v[144:145] op_sel_hi:[1,0]
	v_pk_mul_f32 v[54:55], v[54:55], v[144:145] op_sel_hi:[1,0]
	v_pk_mul_f32 v[58:59], v[52:53], v[144:145] op_sel_hi:[1,0]
	v_pk_mul_f32 v[52:53], v[50:51], v[144:145] op_sel_hi:[1,0]
	v_cvt_pk_bf16_f32 v50, v54, v55
	v_cvt_pk_bf16_f32 v51, v56, v57
	v_cvt_pk_bf16_f32 v52, v52, v53
	v_cvt_pk_bf16_f32 v53, v58, v59
	global_store_dwordx4 v[66:67], v[50:53], off offset:256
	s_or_b64 exec, exec, s[0:1]
	v_cmp_lt_i32_e32 vcc, v142, v179
	s_and_saveexec_b64 s[0:1], vcc
	s_cbranch_execz .LBB0_1487
.LBB0_1494:
	v_ashrrev_i32_e32 v143, 31, v142
	v_lshlrev_b64 v[50:51], 11, v[142:143]
	v_lshl_add_u64 v[50:51], s[18:19], 0, v[50:51]
	s_waitcnt vmcnt(10)
	v_pk_mul_f32 v[48:49], v[48:49], v[140:141] op_sel_hi:[1,0]
	v_pk_mul_f32 v[46:47], v[46:47], v[140:141] op_sel_hi:[1,0]
	v_pk_mul_f32 v[52:53], v[44:45], v[140:141] op_sel_hi:[1,0]
	v_pk_mul_f32 v[44:45], v[42:43], v[140:141] op_sel_hi:[1,0]
	v_lshl_add_u64 v[50:51], v[136:137], 1, v[50:51]
	v_cvt_pk_bf16_f32 v42, v46, v47
	v_cvt_pk_bf16_f32 v43, v48, v49
	v_cvt_pk_bf16_f32 v44, v44, v45
	v_cvt_pk_bf16_f32 v45, v52, v53
	global_store_dwordx4 v[50:51], v[42:45], off
	v_pk_mul_f32 v[40:41], v[40:41], v[140:141] op_sel_hi:[1,0]
	v_pk_mul_f32 v[38:39], v[38:39], v[140:141] op_sel_hi:[1,0]
	v_pk_mul_f32 v[42:43], v[36:37], v[140:141] op_sel_hi:[1,0]
	v_pk_mul_f32 v[36:37], v[34:35], v[140:141] op_sel_hi:[1,0]
	v_cvt_pk_bf16_f32 v34, v38, v39
	v_cvt_pk_bf16_f32 v35, v40, v41
	v_cvt_pk_bf16_f32 v36, v36, v37
	v_cvt_pk_bf16_f32 v37, v42, v43
	global_store_dwordx4 v[50:51], v[34:37], off offset:256
	s_or_b64 exec, exec, s[0:1]
	v_cmp_lt_i32_e32 vcc, v138, v179
	s_and_saveexec_b64 s[0:1], vcc
	s_cbranch_execz .LBB0_1488
.LBB0_1495:
	v_ashrrev_i32_e32 v139, 31, v138
	v_lshlrev_b64 v[34:35], 11, v[138:139]
	v_lshl_add_u64 v[34:35], s[18:19], 0, v[34:35]
	s_waitcnt vmcnt(12)
	v_pk_mul_f32 v[32:33], v[32:33], v[134:135] op_sel_hi:[1,0]
	v_pk_mul_f32 v[30:31], v[30:31], v[134:135] op_sel_hi:[1,0]
	v_pk_mul_f32 v[36:37], v[28:29], v[134:135] op_sel_hi:[1,0]
	v_pk_mul_f32 v[28:29], v[26:27], v[134:135] op_sel_hi:[1,0]
	v_lshl_add_u64 v[34:35], v[136:137], 1, v[34:35]
	v_cvt_pk_bf16_f32 v26, v30, v31
	v_cvt_pk_bf16_f32 v27, v32, v33
	v_cvt_pk_bf16_f32 v28, v28, v29
	v_cvt_pk_bf16_f32 v29, v36, v37
	global_store_dwordx4 v[34:35], v[26:29], off
	v_pk_mul_f32 v[24:25], v[24:25], v[134:135] op_sel_hi:[1,0]
	v_pk_mul_f32 v[22:23], v[22:23], v[134:135] op_sel_hi:[1,0]
	v_pk_mul_f32 v[26:27], v[20:21], v[134:135] op_sel_hi:[1,0]
	v_pk_mul_f32 v[20:21], v[18:19], v[134:135] op_sel_hi:[1,0]
	v_cvt_pk_bf16_f32 v18, v22, v23
	v_cvt_pk_bf16_f32 v19, v24, v25
	v_cvt_pk_bf16_f32 v20, v20, v21
	v_cvt_pk_bf16_f32 v21, v26, v27
	global_store_dwordx4 v[34:35], v[18:21], off offset:256
	s_or_b64 exec, exec, s[0:1]
	v_cmp_lt_i32_e32 vcc, v132, v179
	s_and_saveexec_b64 s[0:1], vcc
	s_cbranch_execz .LBB0_1468
.LBB0_1496:
	v_ashrrev_i32_e32 v133, 31, v132
	v_lshlrev_b64 v[18:19], 11, v[132:133]
	v_lshl_add_u64 v[18:19], s[18:19], 0, v[18:19]
	s_waitcnt vmcnt(14)
	v_pk_mul_f32 v[16:17], v[16:17], v[130:131] op_sel_hi:[1,0]
	v_pk_mul_f32 v[14:15], v[14:15], v[130:131] op_sel_hi:[1,0]
	v_pk_mul_f32 v[20:21], v[12:13], v[130:131] op_sel_hi:[1,0]
	v_pk_mul_f32 v[12:13], v[10:11], v[130:131] op_sel_hi:[1,0]
	v_lshl_add_u64 v[18:19], v[136:137], 1, v[18:19]
	v_cvt_pk_bf16_f32 v10, v14, v15
	v_cvt_pk_bf16_f32 v11, v16, v17
	v_cvt_pk_bf16_f32 v12, v12, v13
	v_cvt_pk_bf16_f32 v13, v20, v21
	global_store_dwordx4 v[18:19], v[10:13], off
	v_pk_mul_f32 v[8:9], v[8:9], v[130:131] op_sel_hi:[1,0]
	v_pk_mul_f32 v[6:7], v[6:7], v[130:131] op_sel_hi:[1,0]
	v_pk_mul_f32 v[10:11], v[4:5], v[130:131] op_sel_hi:[1,0]
	v_pk_mul_f32 v[4:5], v[2:3], v[130:131] op_sel_hi:[1,0]
	v_cvt_pk_bf16_f32 v2, v6, v7
	v_cvt_pk_bf16_f32 v3, v8, v9
	v_cvt_pk_bf16_f32 v4, v4, v5
	v_cvt_pk_bf16_f32 v5, v10, v11
	global_store_dwordx4 v[18:19], v[2:5], off offset:256
	s_branch .LBB0_1468
